# attention ping-pong loops: one static s_setprio 1 for the late (second-on-SIMD) waves during the GQA and differential-attention units, reset after the phase
# baseline (speedup 1.0000x reference)
.LBB0_292:
	v_add_u32_e32 v2, v2, v3
	v_add_u32_e32 v2, v2, v5
	v_add_u32_e32 v2, v2, v4
	v_add_u32_e32 v2, v2, v7
	v_add_u32_e32 v2, v2, v6
	v_add_u32_e32 v2, v2, v9
	v_or_b32_e32 v2, v8, v2
	v_cmp_ne_u32_e32 vcc, 0, v2
	s_and_b64 s[0:1], s[30:31], exec
	s_cselect_b32 s50, 16, 0
	v_cndmask_b32_e64 v2, 0, 1, vcc
	s_mov_b32 s5, s81
	v_readfirstlane_b32 s0, v2
	s_bitcmp1_b32 s0, 0
	s_cselect_b64 s[10:11], -1, 0
	s_xor_b64 s[38:39], s[10:11], -1
	s_lshl_b64 s[0:1], s[4:5], 2
	v_readlane_b32 s2, v254, 42
	s_add_u32 s24, s2, s0
	v_readlane_b32 s2, v254, 43
	s_addc_u32 s25, s2, s1
	s_or_b32 s33, s50, 0x400
	s_barrier
	s_cmp_lg_u64 s[10:11], 0
	s_cbranch_scc0 .Lprio_skip
	s_setprio 1
.Lprio_skip:
	s_mov_b32 s99, 0
	s_branch .LBB0_306

.LBB0_357:
	s_setprio 0
	s_waitcnt vmcnt(0)
	s_waitcnt vmcnt(0) lgkmcnt(0)
	s_barrier
	s_and_saveexec_b64 s[10:11], s[44:45]
	s_cbranch_execz .LBB0_410
	v_readlane_b32 s2, v255, 29
	s_waitcnt vmcnt(0) expcnt(0) lgkmcnt(0)
	s_nop 0
	v_mov_b32_e32 v2, s2
	ds_read_b32 v4, v2
	v_readlane_b32 s2, v255, 30
	s_waitcnt lgkmcnt(0)
	v_cmp_ne_u32_e32 vcc, 0, v4
	v_mov_b32_e32 v2, s2
	ds_read_b32 v2, v2
	s_cbranch_vccnz .LBB0_378
	v_readlane_b32 s4, v253, 16
	v_readlane_b32 s5, v253, 17
	s_load_dwordx2 s[2:3], s[4:5], 0x4
	s_waitcnt lgkmcnt(0)
	s_mul_i32 s2, s2, s86
	s_mul_i32 s2, s2, s3
	s_mov_b32 s3, 1
	s_branch .LBB0_361
